# phase M gate loads issued before the expert-row loop (on v11)
# speedup vs baseline: 1.0002x; 1.0002x over previous
; #define M_UNPACK(dst, v) do { dst[0] = bflo(v.x); dst[1] = bfhi(v.x); dst[2] = bflo(v.y); dst[3] = bfhi(v.y); dst[4] = bflo(v.z); dst[5] = bfhi(v.z); dst[6] = bflo(v.w); dst[7] = bfhi(v.w); } while (0)
; __device__ __forceinline__ void ph_combine(const Params& p, int l) {
;     ...
;         for (int j = 0; j < 4; ++j) { M_UNPACK(x[j], xv[j]);
; #pragma unroll
;             for (int i = 0; i < 8; ++i) s[j][i] = 0.f; }
;         unsigned msk = (unsigned)__ballot(myinv >= 0);
;     ...
;         const float* gate = mod + (size_t)(l * 5 + rr) * 12288 + 5 * DM + lane * 8;
;         float ss = 0.f;
; #pragma unroll
;         for (int j = 0; j < 4; ++j) { const f32x4 g0 = *(const f32x4*)(gate + j * 512), g1 = *(const f32x4*)(gate + j * 512 + 4);
.LBB0_2685:
	v_lshl_add_u32 v180, s25, 3, v124
	v_min_i32_e32 v180, 0x2000, v180
	v_ashrrev_i32_e32 v180, 11, v180
	v_add_u32_e32 v180, s13, v180
	v_mul_hi_i32_i24_e32 v181, 0xc000, v180
	v_mul_i32_i24_e32 v180, 0xc000, v180
	v_lshl_add_u64 v[180:181], s[2:3], 0, v[180:181]
	v_lshl_add_u64 v[180:181], v[180:181], 0, v[206:207]
	s_mov_b64 s[0:1], 0xa000
	v_lshl_add_u64 v[182:183], v[180:181], 0, s[0:1]
	s_mov_b32 s0, 0xb000
	v_add_co_u32_e32 v184, vcc, s0, v180
	s_nop 1
	v_addc_co_u32_e32 v185, vcc, 0, v181, vcc
	global_load_dwordx4 v[148:151], v[184:185], off offset:-4096
	global_load_dwordx4 v[152:155], v[182:183], off offset:16
	global_load_dwordx4 v[156:159], v[182:183], off offset:2064
	global_load_dwordx4 v[160:163], v[182:183], off offset:2048
	global_load_dwordx4 v[164:167], v[184:185], off
	global_load_dwordx4 v[168:171], v[184:185], off offset:16
	global_load_dwordx4 v[172:175], v[184:185], off offset:2048
	global_load_dwordx4 v[176:179], v[184:185], off offset:2064
	v_cmp_lt_i32_e32 vcc, -1, v92
	s_cmp_eq_u32 vcc_lo, 0
	s_cbranch_scc1 .LBB0_2688
	v_mov_b32_e32 v58, 0
	v_mov_b32_e32 v59, v58
	v_mov_b32_e32 v60, v58
	v_mov_b32_e32 v61, v58
	v_mov_b32_e32 v88, v58
	v_mov_b32_e32 v89, v58
	v_mov_b32_e32 v90, v58
	v_mov_b32_e32 v91, v58
	v_mov_b32_e32 v50, v58
	v_mov_b32_e32 v51, v58
	v_mov_b32_e32 v52, v58
	v_mov_b32_e32 v53, v58
	v_mov_b32_e32 v54, v58
	v_mov_b32_e32 v55, v58
	v_mov_b32_e32 v56, v58
	v_mov_b32_e32 v57, v58
	v_mov_b32_e32 v42, v58
	v_mov_b32_e32 v43, v58
	v_mov_b32_e32 v44, v58
	v_mov_b32_e32 v45, v58
	v_mov_b32_e32 v46, v58
	v_mov_b32_e32 v47, v58
	v_mov_b32_e32 v48, v58
	v_mov_b32_e32 v49, v58
	v_mov_b32_e32 v34, v58
	v_mov_b32_e32 v35, v58
	v_mov_b32_e32 v36, v58
	v_mov_b32_e32 v37, v58
	v_mov_b32_e32 v38, v58
	v_mov_b32_e32 v39, v58
	v_mov_b32_e32 v40, v58
	v_mov_b32_e32 v41, v58

; __device__ __forceinline__ void ph_combine(const Params& p, int l) {
;     ...
;         const float* gate = mod + (size_t)(l * 5 + rr) * 12288 + 5 * DM + lane * 8;
;         float ss = 0.f;
; #pragma unroll
;         for (int j = 0; j < 4; ++j) { const f32x4 g0 = *(const f32x4*)(gate + j * 512), g1 = *(const f32x4*)(gate + j * 512 + 4);
; #pragma unroll
;             for (int i = 0; i < 8; ++i) { x[j][i] += (i < 4 ? g0[i] : g1[i - 4]) * s[j][i]; ss += x[j][i] * x[j][i]; } }
;         ss = wave_sum(ss); const float rinv = rsqrtf(ss * (1.0f / DM) + EPS);
.LBB0_2689:
	v_lshlrev_b32_e32 v118, 16, v30
	v_and_b32_e32 v119, 0xffff0000, v30
	v_lshl_add_u32 v30, s25, 3, v124
	v_lshlrev_b32_e32 v116, 16, v32
	v_and_b32_e32 v117, 0xffff0000, v32
	v_lshlrev_b32_e32 v114, 16, v33
	v_and_b32_e32 v115, 0xffff0000, v33
	v_lshlrev_b32_e32 v32, 16, v20
	v_and_b32_e32 v33, 0xffff0000, v20
	v_min_i32_e32 v20, 0x2000, v30
	v_ashrrev_i32_e32 v120, 11, v20
	v_add_u32_e32 v20, s13, v120
	v_lshlrev_b32_e32 v98, 16, v18
	v_and_b32_e32 v99, 0xffff0000, v18
	v_lshlrev_b32_e32 v96, 16, v19
	v_and_b32_e32 v97, 0xffff0000, v19
	v_lshlrev_b32_e32 v18, 16, v21
	v_and_b32_e32 v19, 0xffff0000, v21
	v_mul_hi_i32_i24_e32 v21, 0xc000, v20
	v_mul_i32_i24_e32 v20, 0xc000, v20
	v_lshl_add_u64 v[20:21], s[2:3], 0, v[20:21]
	v_lshl_add_u64 v[122:123], v[20:21], 0, v[206:207]
	s_mov_b64 s[0:1], 0xa000
	v_lshl_add_u64 v[138:139], v[122:123], 0, s[0:1]
	s_mov_b32 s0, 0xb000
	v_add_co_u32_e32 v140, vcc, s0, v122
	v_lshlrev_b32_e32 v94, 16, v22
	s_nop 0
	v_addc_co_u32_e32 v141, vcc, 0, v123, vcc
	v_and_b32_e32 v95, 0xffff0000, v22
	v_lshlrev_b32_e32 v92, 16, v23
	v_and_b32_e32 v93, 0xffff0000, v23
	v_lshlrev_b32_e32 v108, 16, v31
	v_and_b32_e32 v109, 0xffff0000, v31
	v_lshlrev_b32_e32 v112, 16, v26
	v_and_b32_e32 v113, 0xffff0000, v26
	v_lshlrev_b32_e32 v110, 16, v27
	v_and_b32_e32 v111, 0xffff0000, v27
	v_lshlrev_b32_e32 v106, 16, v28
	v_and_b32_e32 v107, 0xffff0000, v28
	v_lshlrev_b32_e32 v104, 16, v29
	v_and_b32_e32 v105, 0xffff0000, v29
	v_lshlrev_b32_e32 v102, 16, v24
	v_and_b32_e32 v103, 0xffff0000, v24
	v_lshlrev_b32_e32 v100, 16, v25
	v_and_b32_e32 v101, 0xffff0000, v25
	s_mov_b64 s[0:1], 0xb000
	v_readlane_b32 s14, v255, 57
	v_readlane_b32 s15, v255, 58
	v_ashrrev_i32_e32 v31, 31, v30
	s_waitcnt vmcnt(7)
	v_pk_fma_f32 v[28:29], v[90:91], v[148:149], v[118:119]
	v_pk_fma_f32 v[26:27], v[88:89], v[150:151], v[108:109]
	s_waitcnt vmcnt(6)
	v_pk_fma_f32 v[24:25], v[60:61], v[152:153], v[116:117]
	v_pk_fma_f32 v[22:23], v[58:59], v[154:155], v[114:115]
	v_pk_mul_f32 v[20:21], v[28:29], v[28:29]
	v_pk_mul_f32 v[108:109], v[26:27], v[26:27]
	v_add_f32_e32 v20, v20, v21
	v_add_f32_e32 v20, v108, v20
	v_pk_mul_f32 v[60:61], v[24:25], v[24:25]
	v_add_f32_e32 v20, v109, v20
	v_add_f32_e32 v20, v60, v20
	v_pk_mul_f32 v[58:59], v[22:23], v[22:23]
	v_add_f32_e32 v20, v61, v20
	v_add_f32_e32 v20, v58, v20
	v_add_f32_e32 v20, v59, v20
	s_waitcnt vmcnt(5)
	v_pk_fma_f32 v[106:107], v[52:53], v[156:157], v[106:107]
	s_waitcnt vmcnt(4)
	v_pk_fma_f32 v[112:113], v[56:57], v[160:161], v[112:113]
	v_lshl_add_u64 v[114:115], v[122:123], 0, s[0:1]
	v_pk_fma_f32 v[110:111], v[54:55], v[162:163], v[110:111]
	v_pk_fma_f32 v[104:105], v[50:51], v[158:159], v[104:105]
	s_nop 0
	s_mov_b64 s[0:1], 0xb800
	v_pk_mul_f32 v[56:57], v[112:113], v[112:113]
	v_pk_mul_f32 v[54:55], v[110:111], v[110:111]
	v_add_f32_e32 v20, v56, v20
	v_add_f32_e32 v20, v57, v20
	v_add_f32_e32 v20, v54, v20
	v_pk_mul_f32 v[52:53], v[106:107], v[106:107]
	v_add_f32_e32 v20, v55, v20
	v_add_f32_e32 v20, v52, v20
	v_pk_mul_f32 v[50:51], v[104:105], v[104:105]
	v_add_f32_e32 v20, v53, v20
	v_add_f32_e32 v20, v50, v20
	v_add_f32_e32 v20, v51, v20
	s_waitcnt vmcnt(3)
	v_pk_fma_f32 v[92:93], v[46:47], v[166:167], v[92:93]
	s_waitcnt vmcnt(2)
	v_pk_fma_f32 v[90:91], v[44:45], v[168:169], v[102:103]
	v_lshl_add_u64 v[114:115], v[122:123], 0, s[0:1]
	v_pk_fma_f32 v[94:95], v[48:49], v[164:165], v[94:95]
	v_pk_fma_f32 v[88:89], v[42:43], v[170:171], v[100:101]
	s_nop 0
	v_pk_mul_f32 v[48:49], v[94:95], v[94:95]
	v_pk_mul_f32 v[46:47], v[92:93], v[92:93]
	v_add_f32_e32 v20, v48, v20
	v_add_f32_e32 v20, v49, v20
	v_add_f32_e32 v20, v46, v20
	v_pk_mul_f32 v[44:45], v[90:91], v[90:91]
	v_add_f32_e32 v20, v47, v20
	v_add_f32_e32 v20, v44, v20
	v_pk_mul_f32 v[42:43], v[88:89], v[88:89]
	v_add_f32_e32 v20, v45, v20
	v_add_f32_e32 v20, v42, v20
	v_add_f32_e32 v20, v43, v20
	s_mov_b32 s0, 0x800000
	s_waitcnt vmcnt(1)
	v_pk_fma_f32 v[98:99], v[40:41], v[172:173], v[98:99]
	s_nop 0
	v_pk_mul_f32 v[40:41], v[98:99], v[98:99]
	v_pk_fma_f32 v[96:97], v[38:39], v[174:175], v[96:97]
	v_add_f32_e32 v20, v40, v20
	v_pk_mul_f32 v[38:39], v[96:97], v[96:97]
	v_add_f32_e32 v20, v41, v20
	s_waitcnt vmcnt(0)
	v_pk_fma_f32 v[102:103], v[36:37], v[176:177], v[32:33]
	v_add_f32_e32 v20, v38, v20
	v_pk_mul_f32 v[32:33], v[102:103], v[102:103]
	v_add_f32_e32 v20, v39, v20
	v_pk_fma_f32 v[100:101], v[34:35], v[178:179], v[18:19]
	v_add_f32_e32 v20, v32, v20
	v_pk_mul_f32 v[18:19], v[100:101], v[100:101]
	v_add_f32_e32 v20, v33, v20
	v_add_f32_e32 v18, v18, v20
	v_add_f32_e32 v18, v19, v18
	v_mov_b32_e32 v19, v18
	s_nop 1
	v_permlane32_swap_b32_e32 v19, v18
	s_waitcnt lgkmcnt(0)
	v_add_f32_e32 v18, v18, v19
	v_mov_b32_e32 v19, v18
	s_nop 1
	v_permlane16_swap_b32_e32 v19, v18
	s_waitcnt lgkmcnt(0)
	v_add_f32_e32 v18, v18, v19
	s_nop 1
	v_mov_b32_dpp v19, v18 row_ror:8 row_mask:0xf bank_mask:0xf
	s_waitcnt lgkmcnt(0)
	v_add_f32_e32 v18, v18, v19
	s_nop 1
	v_mov_b32_dpp v19, v18 row_shl:4 row_mask:0xf bank_mask:0x5
	v_mov_b32_dpp v19, v18 row_shr:4 row_mask:0xf bank_mask:0xa
	s_waitcnt lgkmcnt(0)
	v_add_f32_e32 v18, v18, v19
	s_nop 1
	v_mov_b32_dpp v19, v18 quad_perm:[2,3,0,1] row_mask:0xf bank_mask:0xf
	s_waitcnt lgkmcnt(0)
	v_add_f32_e32 v18, v18, v19
	s_nop 1
	v_mov_b32_dpp v19, v18 quad_perm:[1,0,3,2] row_mask:0xf bank_mask:0xf
	s_waitcnt lgkmcnt(0)
	v_add_f32_e32 v18, v18, v19
	v_fmamk_f32 v18, v18, 0x3a000000, v246
	v_cmp_gt_f32_e32 vcc, s0, v18
	v_mul_f32_e32 v19, 0x4b800000, v18
	s_mov_b64 s[0:1], -1
	v_cndmask_b32_e32 v18, v18, v19, vcc
	v_rsq_f32_e32 v18, v18
	s_nop 0
	v_mul_f32_e32 v19, 0x45800000, v18
	v_cndmask_b32_e32 v108, v18, v19, vcc
	s_and_b64 vcc, exec, s[14:15]
	s_cbranch_vccz .LBB0_2691
; __device__ __forceinline__ void ph_combine(const Params& p, int l) {
;     ...
;         } else {
;             float* orow = p.out + (size_t)row * DM + lane * 8; const float* g = p.in[I_FNG] + lane * 8;
;             f32x4 gq[8];
; #pragma unroll
;             for (int j = 0; j < 4; ++j) { gq[2 * j] = *(const f32x4*)(g + j * 512); gq[2 * j + 1] = *(const f32x4*)(g + j * 512 + 4); }
; #pragma unroll
;             for (int j = 0; j < 4; ++j) { const f32x4 ga = gq[2 * j], gb = gq[2 * j + 1];
;                 *(f32x4*)(orow + j * 512) = (f32x4){x[j][0] * rinv * ga[0], x[j][1] * rinv * ga[1], x[j][2] * rinv * ga[2], x[j][3] * rinv * ga[3]};
;                 *(f32x4*)(orow + j * 512 + 4) = (f32x4){x[j][4] * rinv * gb[0], x[j][5] * rinv * gb[1], x[j][6] * rinv * gb[2], x[j][7] * rinv * gb[3]}; }
	global_load_dwordx4 v[32:35], v[76:77], off offset:16
	global_load_dwordx4 v[36:39], v[76:77], off
	global_load_dwordx4 v[40:43], v[76:77], off offset:2064
	global_load_dwordx4 v[44:47], v[76:77], off offset:2048
	global_load_dwordx4 v[48:51], v[78:79], off offset:16
	global_load_dwordx4 v[52:55], v[78:79], off
	global_load_dwordx4 v[18:21], v[80:81], off offset:16
	global_load_dwordx4 v[56:59], v[80:81], off
	v_lshlrev_b64 v[60:61], 13, v[30:31]
	v_pk_mul_f32 v[114:115], v[28:29], v[108:109] op_sel_hi:[1,0]
	v_pk_mul_f32 v[116:117], v[26:27], v[108:109] op_sel_hi:[1,0]
	v_lshl_add_u64 v[60:61], v[74:75], 0, v[60:61]
	s_movk_i32 s0, 0x1000
	s_waitcnt vmcnt(6)
	v_pk_mul_f32 v[38:39], v[116:117], v[38:39]
	v_pk_mul_f32 v[36:37], v[114:115], v[36:37]
	global_store_dwordx4 v[60:61], v[36:39], off
	s_nop 1
	v_pk_mul_f32 v[36:37], v[24:25], v[108:109] op_sel_hi:[1,0]
	v_pk_mul_f32 v[38:39], v[22:23], v[108:109] op_sel_hi:[1,0]
	v_pk_mul_f32 v[32:33], v[36:37], v[32:33]
	v_pk_mul_f32 v[34:35], v[38:39], v[34:35]
	global_store_dwordx4 v[60:61], v[32:35], off offset:16
	v_add_co_u32_e32 v36, vcc, s0, v60
	s_nop 0
	v_pk_mul_f32 v[32:33], v[112:113], v[108:109] op_sel_hi:[1,0]
	v_pk_mul_f32 v[34:35], v[110:111], v[108:109] op_sel_hi:[1,0]
	s_waitcnt vmcnt(6)
	v_pk_mul_f32 v[32:33], v[32:33], v[44:45]
	v_pk_mul_f32 v[34:35], v[34:35], v[46:47]
	global_store_dwordx4 v[60:61], v[32:35], off offset:2048
	v_addc_co_u32_e32 v37, vcc, 0, v61, vcc
	s_nop 0
	v_pk_mul_f32 v[32:33], v[106:107], v[108:109] op_sel_hi:[1,0]
	v_pk_mul_f32 v[34:35], v[104:105], v[108:109] op_sel_hi:[1,0]
	v_pk_mul_f32 v[32:33], v[32:33], v[40:41]
	v_pk_mul_f32 v[34:35], v[34:35], v[42:43]
	global_store_dwordx4 v[60:61], v[32:35], off offset:2064
	s_mov_b64 s[0:1], 0
	s_nop 0
	v_pk_mul_f32 v[32:33], v[94:95], v[108:109] op_sel_hi:[1,0]
	v_pk_mul_f32 v[34:35], v[92:93], v[108:109] op_sel_hi:[1,0]
	s_waitcnt vmcnt(6)
	v_pk_mul_f32 v[32:33], v[32:33], v[52:53]
	v_pk_mul_f32 v[34:35], v[34:35], v[54:55]
	global_store_dwordx4 v[36:37], v[32:35], off
	s_nop 1
	v_pk_mul_f32 v[32:33], v[90:91], v[108:109] op_sel_hi:[1,0]
	v_pk_mul_f32 v[34:35], v[88:89], v[108:109] op_sel_hi:[1,0]
	v_pk_mul_f32 v[32:33], v[32:33], v[48:49]
	v_pk_mul_f32 v[34:35], v[34:35], v[50:51]
	global_store_dwordx4 v[36:37], v[32:35], off offset:16
	s_nop 1
	v_pk_mul_f32 v[32:33], v[98:99], v[108:109] op_sel_hi:[1,0]
	v_pk_mul_f32 v[34:35], v[96:97], v[108:109] op_sel_hi:[1,0]
	s_waitcnt vmcnt(6)
	v_pk_mul_f32 v[32:33], v[32:33], v[56:57]
	v_pk_mul_f32 v[34:35], v[34:35], v[58:59]
	global_store_dwordx4 v[36:37], v[32:35], off offset:2048
	s_nop 1
	v_pk_mul_f32 v[32:33], v[102:103], v[108:109] op_sel_hi:[1,0]
	v_pk_mul_f32 v[34:35], v[100:101], v[108:109] op_sel_hi:[1,0]
	v_pk_mul_f32 v[18:19], v[32:33], v[18:19]
	v_pk_mul_f32 v[20:21], v[34:35], v[20:21]
	global_store_dwordx4 v[36:37], v[18:21], off offset:2064
